# sparse L0 tile loop: hoisted K-read addresses and ones operand, shift-based next-tile query index, packed max-shift and 64-bit bias refresh (on top of L1 dense dword-store epilogue + L0 sparse bias ta
# baseline (speedup 1.0000x reference)
; #define SBAR() __builtin_amdgcn_sched_barrier(0)
; #define SBAR() __builtin_amdgcn_sched_barrier(0)
; #define SP8_DMA_V(T) do { const unsigned char* vb_ = SP8_UNI((T).v); \
;         _Pragma("unroll") for (int i = 0; i < 8; ++i) { const unsigned char* src = vb_ + (unsigned long long)(16 * i) * SEQ + voff; \
;         __builtin_amdgcn_global_load_lds((const unsigned*)src, (LAS unsigned*)(wll + 8192 + i * 1024), 16, 0, 0); } } while (0)
; template <class P>
; __device__ __forceinline__ void sparse8_wave(P& pol, LAS unsigned char* wll, int lane) {
;     ...
;     const int a0k = 32 * ((lane >> 5) & 1) + ((lane >> 3) & 3), che = (((lane & 7) ^ (lane >> 4)) & 7) << 4, cho = che ^ 64;
;     const int vcol0 = lane >> 2; const unsigned voff = (unsigned)vcol0 * SEQ + ((((lane & 3) ^ (vcol0 >> 2)) & 3) << 4);
;     const int nt = pol.ntiles();
;     typename P::TI ti, tn;
;     ...
;     pol.tile(0, ti);
;     SP8_DMA_K(ti); SP8_DMA_V(ti);
;     pol.pre_issue(); SBAR();
;     i32x8 qf[2];
;     { const bf16_t* Qw = pol.qptr(r32); u32x4 qv[2][4];
; #pragma unroll
;       for (int sK = 0; sK < 2; ++sK)
; #pragma unroll
;           for (int c = 0; c < 4; ++c) qv[sK][c] = *(const u32x4*)(Qw + 64 * sK + 32 * hi + 8 * c);
;     __device__ __forceinline__ void tile(int j, TI& ti) const {
;         int dil, kt, rd; const unsigned char* vt; int voff;
;         if (j < n3) { dil = 16; kt = lo3 + j; rd = r16; vt = Vt16; voff = r16 * 256 + 64 * kt; }
;         else if (j < n3 + n2) { dil = 4; kt = lo2 + (j - n3); rd = r16 & 3; vt = Vt4; voff = rd * 1024 + 64 * kt; }
;         else { dil = 1; kt = lo1 + (j - n3 - n2); rd = 0; vt = Vt1; voff = 64 * kt; }
;         const long tok = (long)b * SEQ + dil * 64 * kt + rd;
;         ti.k = K8 + tok * 1024 + h * 128; ti.rs = (long)dil * 1024; ti.v = vt + (long)(b * 8 + h) * 128 * SEQ + voff;
;         ti.fb = (float)(64 * kt + hi32 - (512 * a + r16 + 16 * myn - rd) / dil); ti.ncd = -slope2 * (float)dil;
.LBB0_553:
	v_and_b32_e32 v163, 63, v32
	v_and_b32_e32 v165, 32, v32
	v_lshrrev_b32_e32 v0, 3, v32
	s_mul_i32 s0, s8, 0x4900
	v_and_or_b32 v166, v0, 3, v165
	v_lshlrev_b32_e32 v0, 4, v163
	s_add_i32 s61, s0, 0
	s_ashr_i32 s0, s33, 10
	s_bfe_u32 s38, s33, 0x30007
	s_min_u32 s1, s41, 55
	v_bitop3_b32 v34, v0, v32, 63 bitop3:0x78
	v_bitop3_b32 v167, v0, s89, v163 bitop3:0x48
	v_lshlrev_b32_e32 v0, 10, v32
	s_mov_b32 s33, 0xf030
	v_bitop3_b32 v232, v34, s33, v0 bitop3:0xc8
	s_sub_i32 s1, s1, s42
	s_mul_i32 s33, s29, s24
	s_add_i32 s62, s1, s60
	s_ashr_i32 s1, s0, 31
	s_add_i32 s36, s33, s25
	s_add_i32 s62, s62, 10
	s_lshl_b64 s[42:43], s[0:1], 22
	s_lshl_b64 s[48:49], s[36:37], 10
	s_add_u32 s1, s52, s42
	s_addc_u32 s33, s53, s43
	s_add_u32 s41, s1, s48
	s_addc_u32 s43, s33, s49
	s_lshl_b32 s36, s38, 7
	s_add_u32 s42, s41, s36
	s_addc_u32 s43, s43, 0
	s_lshl_b32 s41, s0, 3
	s_or_b32 s48, s38, s41
	s_ashr_i32 s49, s48, 31
	s_lshl_b64 s[72:73], s[48:49], 19
	v_mul_lo_u32 v0, s29, v166
	s_lshl_b32 s41, s29, 12
	v_lshlrev_b32_e32 v0, 10, v0
	s_add_u32 s48, s42, s41
	v_or_b32_e32 v1, v0, v167
	s_mov_b32 m0, s61
	s_addc_u32 s49, s43, 0
	s_add_i32 s63, s61, 0x400
	global_load_lds_dwordx4 v1, s[42:43]
	v_bitop3_b32 v0, v0, v167, 64 bitop3:0xf6
	s_mov_b32 m0, s63
	s_lshl_b32 s41, s29, 13
	global_load_lds_dwordx4 v0, s[48:49]
	s_add_u32 s48, s42, s41
	s_addc_u32 s49, s43, 0
	s_add_i32 s64, s61, 0x800
	s_mov_b32 m0, s64
	s_mul_i32 s41, s29, 0x3000
	global_load_lds_dwordx4 v1, s[48:49]
	s_add_u32 s48, s42, s41
	s_addc_u32 s49, s43, 0
	s_add_i32 s65, s61, 0xc00
	s_mov_b32 m0, s65
	s_lshl_b32 s41, s29, 14
	global_load_lds_dwordx4 v0, s[48:49]
	s_add_u32 s48, s42, s41
	s_addc_u32 s49, s43, 0
	s_add_i32 s66, s61, 0x1000
	s_mov_b32 m0, s66
	s_mul_i32 s41, s29, 0x5000
	global_load_lds_dwordx4 v1, s[48:49]
	s_add_u32 s48, s42, s41
	s_addc_u32 s49, s43, 0
	s_add_i32 s67, s61, 0x1400
	s_mov_b32 m0, s67
	s_mul_i32 s41, s29, 0x6000
	global_load_lds_dwordx4 v0, s[48:49]
	s_add_u32 s48, s42, s41
	s_addc_u32 s49, s43, 0
	s_add_i32 s86, s61, 0x1800
	s_mul_i32 s41, s29, 0x7000
	s_add_u32 s42, s42, s41
	s_addc_u32 s43, s43, 0
	s_add_i32 s87, s61, 0x1c00
	s_add_u32 s6, s6, s72
	s_addc_u32 s7, s7, s73
	s_mov_b32 m0, s86
	s_add_u32 s6, s6, s40
	global_load_lds_dwordx4 v1, s[48:49]
	s_mov_b32 m0, s87
	s_addc_u32 s7, s7, 0
	s_add_i32 s92, s61, 0x2000
	global_load_lds_dwordx4 v0, s[42:43]
	s_mov_b32 m0, s92
	v_lshl_add_u64 v[0:1], s[6:7], 0, v[232:233]
	global_load_lds_dwordx4 v232, s[6:7]
	s_mov_b64 s[6:7], 0x10000
	s_add_i32 s93, s61, 0x2400
	v_lshl_add_u64 v[2:3], v[0:1], 0, s[6:7]
	s_mov_b32 m0, s93
	s_add_i32 s94, s61, 0x2800
	global_load_lds_dwordx4 v[2:3], off
	v_lshl_add_u64 v[2:3], v[0:1], 0, s[26:27]
	s_mov_b32 m0, s94
	s_mov_b64 s[6:7], 0x30000
	s_add_i32 s95, s61, 0x2c00
	global_load_lds_dwordx4 v[2:3], off
	v_lshl_add_u64 v[2:3], v[0:1], 0, s[6:7]
	s_mov_b32 m0, s95
	s_mov_b64 s[6:7], 0x40000
	s_add_i32 s96, s61, 0x3000
	global_load_lds_dwordx4 v[2:3], off
	v_lshl_add_u64 v[2:3], v[0:1], 0, s[6:7]
	s_mov_b32 m0, s96
	s_mov_b64 s[6:7], 0x50000
	s_add_i32 s97, s61, 0x3400
	global_load_lds_dwordx4 v[2:3], off
	v_lshl_add_u64 v[2:3], v[0:1], 0, s[6:7]
	s_mov_b32 m0, s97
	s_mov_b64 s[6:7], 0x60000
	s_add_i32 s48, s61, 0x3800
	global_load_lds_dwordx4 v[2:3], off
	v_lshl_add_u64 v[2:3], v[0:1], 0, s[6:7]
	s_mov_b32 m0, s48
	s_mov_b64 s[6:7], 0x70000
	s_add_i32 s49, s61, 0x3c00
	global_load_lds_dwordx4 v[2:3], off
	v_lshl_add_u64 v[0:1], v[0:1], 0, s[6:7]
	s_mov_b32 m0, s49
	v_and_b32_e32 v160, 31, v32
	global_load_lds_dwordx4 v[0:1], off
	v_bfe_u32 v161, v32, 5, 1
	s_lshl_b32 s58, s0, 12
	v_lshl_or_b32 v33, v160, 4, s15
	s_lshl_b32 s57, s39, 9
	v_or_b32_e32 v0, s58, v33
	v_or_b32_e32 v2, s57, v0
	v_mov_b64_e32 v[0:1], s[68:69]
	s_movk_i32 s0, 0x2400
	v_mad_i64_i32 v[0:1], s[6:7], v2, s0, v[0:1]
	s_lshl_b32 s6, s38, 8
	s_mov_b32 s7, s37
	v_lshl_add_u64 v[0:1], v[0:1], 0, s[6:7]
	v_lshlrev_b32_e32 v2, 1, v165
	v_mov_b32_e32 v3, v233
	v_lshl_add_u64 v[12:13], v[0:1], 0, v[2:3]
	global_load_dwordx4 v[16:19], v[12:13], off offset:3120
	global_load_dwordx4 v[20:23], v[12:13], off offset:3104
	global_load_dwordx4 v[24:27], v[12:13], off offset:3088
	global_load_dwordx4 v[28:31], v[12:13], off offset:3072
	global_load_dwordx4 v[0:3], v[12:13], off offset:3248
	global_load_dwordx4 v[4:7], v[12:13], off offset:3232
	global_load_dwordx4 v[8:11], v[12:13], off offset:3216
	s_nop 0
	global_load_dwordx4 v[12:15], v[12:13], off offset:3200
	s_cmp_lt_i32 s62, 1
	s_cbranch_scc1 .LBB0_579
; __device__ __forceinline__ float bflo(unsigned w) { return __uint_as_float(w << 16); }
; __device__ __forceinline__ float bfhi(unsigned w) { return __uint_as_float(w & 0xffff0000u); }
; template <class P>
; __device__ __forceinline__ void sparse8_wave(P& pol, LAS unsigned char* wll, int lane) {
;     ...
; #pragma unroll
;       for (int sK = 0; sK < 2; ++sK) { unsigned w[8];
; #pragma unroll
;           for (int c = 0; c < 4; ++c) { const u32x4 v = qv[sK][c];
;               w[2 * c] = pk4_fp8(bflo(v.x) * QCS, bfhi(v.x) * QCS, bflo(v.y) * QCS, bfhi(v.y) * QCS); w[2 * c + 1] = pk4_fp8(bflo(v.z) * QCS, bfhi(v.z) * QCS, bflo(v.w) * QCS, bfhi(v.w) * QCS); }
;           qf[sK] = (i32x8){(int)w[0], (int)w[1], (int)w[2], (int)w[3], (int)w[4], (int)w[5], (int)w[6], (int)w[7]}; } }
	v_mov_b32_e32 v35, 0x70
	v_bitop3_b32 v168, v34, 64, v35 bitop3:0x6c
	s_waitcnt vmcnt(0)
	v_lshlrev_b32_e32 v34, 16, v28
	v_and_b32_e32 v28, 0xffff0000, v28
	v_mul_f32_e32 v128, 0x3e0293ee, v34
	v_mul_f32_e32 v28, 0x3e0293ee, v28
	v_cvt_pk_fp8_f32 v128, v128, v28
	v_lshlrev_b32_e32 v34, 16, v29
	v_and_b32_e32 v29, 0xffff0000, v29
	v_mul_f32_e32 v28, 0x3e0293ee, v34
	v_mul_f32_e32 v29, 0x3e0293ee, v29
	v_cvt_pk_fp8_f32 v128, v28, v29 op_sel:[0,0,1]
	v_lshlrev_b32_e32 v28, 16, v30
	v_mul_f32_e32 v129, 0x3e0293ee, v28
	v_and_b32_e32 v28, 0xffff0000, v30
	v_mul_f32_e32 v28, 0x3e0293ee, v28
	v_cvt_pk_fp8_f32 v129, v129, v28
	v_lshlrev_b32_e32 v29, 16, v31
	v_mul_f32_e32 v28, 0x3e0293ee, v29
	v_and_b32_e32 v29, 0xffff0000, v31
	v_mul_f32_e32 v29, 0x3e0293ee, v29
	v_cvt_pk_fp8_f32 v129, v28, v29 op_sel:[0,0,1]
	v_lshlrev_b32_e32 v28, 16, v24
	v_and_b32_e32 v24, 0xffff0000, v24
	v_mul_f32_e32 v130, 0x3e0293ee, v28
	v_mul_f32_e32 v24, 0x3e0293ee, v24
	v_cvt_pk_fp8_f32 v130, v130, v24
	v_lshlrev_b32_e32 v28, 16, v25
	v_and_b32_e32 v25, 0xffff0000, v25
	v_mul_f32_e32 v24, 0x3e0293ee, v28
	v_mul_f32_e32 v25, 0x3e0293ee, v25
	v_cvt_pk_fp8_f32 v130, v24, v25 op_sel:[0,0,1]
	v_lshlrev_b32_e32 v24, 16, v26
	v_mul_f32_e32 v131, 0x3e0293ee, v24
	v_and_b32_e32 v24, 0xffff0000, v26
	v_mul_f32_e32 v24, 0x3e0293ee, v24
	v_cvt_pk_fp8_f32 v131, v131, v24
	v_lshlrev_b32_e32 v25, 16, v27
	v_mul_f32_e32 v24, 0x3e0293ee, v25
	v_and_b32_e32 v25, 0xffff0000, v27
	v_mul_f32_e32 v25, 0x3e0293ee, v25
	v_cvt_pk_fp8_f32 v131, v24, v25 op_sel:[0,0,1]
	v_lshlrev_b32_e32 v24, 16, v20
	v_and_b32_e32 v20, 0xffff0000, v20
	v_mul_f32_e32 v132, 0x3e0293ee, v24
	v_mul_f32_e32 v20, 0x3e0293ee, v20
	v_cvt_pk_fp8_f32 v132, v132, v20
	v_lshlrev_b32_e32 v24, 16, v21
	v_and_b32_e32 v21, 0xffff0000, v21
	v_mul_f32_e32 v20, 0x3e0293ee, v24
	v_mul_f32_e32 v21, 0x3e0293ee, v21
	v_cvt_pk_fp8_f32 v132, v20, v21 op_sel:[0,0,1]
	v_lshlrev_b32_e32 v20, 16, v22
	v_mul_f32_e32 v133, 0x3e0293ee, v20
	v_and_b32_e32 v20, 0xffff0000, v22
	v_mul_f32_e32 v20, 0x3e0293ee, v20
	v_cvt_pk_fp8_f32 v133, v133, v20
	v_lshlrev_b32_e32 v21, 16, v23
	v_mul_f32_e32 v20, 0x3e0293ee, v21
	v_and_b32_e32 v21, 0xffff0000, v23
	v_mul_f32_e32 v21, 0x3e0293ee, v21
	v_cvt_pk_fp8_f32 v133, v20, v21 op_sel:[0,0,1]
	v_lshlrev_b32_e32 v20, 16, v16
	v_and_b32_e32 v16, 0xffff0000, v16
	v_mul_f32_e32 v134, 0x3e0293ee, v20
	v_mul_f32_e32 v16, 0x3e0293ee, v16
	v_cvt_pk_fp8_f32 v134, v134, v16
	v_lshlrev_b32_e32 v20, 16, v17
	v_and_b32_e32 v17, 0xffff0000, v17
	v_mul_f32_e32 v16, 0x3e0293ee, v20
	v_mul_f32_e32 v17, 0x3e0293ee, v17
	v_cvt_pk_fp8_f32 v134, v16, v17 op_sel:[0,0,1]
	v_lshlrev_b32_e32 v16, 16, v18
	v_mul_f32_e32 v135, 0x3e0293ee, v16
	v_and_b32_e32 v16, 0xffff0000, v18
	v_mul_f32_e32 v16, 0x3e0293ee, v16
	v_cvt_pk_fp8_f32 v135, v135, v16
	v_lshlrev_b32_e32 v17, 16, v19
	v_mul_f32_e32 v16, 0x3e0293ee, v17
	v_and_b32_e32 v17, 0xffff0000, v19
	v_mul_f32_e32 v17, 0x3e0293ee, v17
	v_cvt_pk_fp8_f32 v135, v16, v17 op_sel:[0,0,1]
	v_lshlrev_b32_e32 v16, 16, v12
	v_and_b32_e32 v12, 0xffff0000, v12
	v_mul_f32_e32 v136, 0x3e0293ee, v16
	v_mul_f32_e32 v12, 0x3e0293ee, v12
	v_cvt_pk_fp8_f32 v136, v136, v12
	v_lshlrev_b32_e32 v16, 16, v13
	v_and_b32_e32 v13, 0xffff0000, v13
	v_mul_f32_e32 v12, 0x3e0293ee, v16
	v_mul_f32_e32 v13, 0x3e0293ee, v13
	v_cvt_pk_fp8_f32 v136, v12, v13 op_sel:[0,0,1]
	v_lshlrev_b32_e32 v12, 16, v14
	v_mul_f32_e32 v137, 0x3e0293ee, v12
	v_and_b32_e32 v12, 0xffff0000, v14
	v_mul_f32_e32 v12, 0x3e0293ee, v12
	v_cvt_pk_fp8_f32 v137, v137, v12
	v_lshlrev_b32_e32 v13, 16, v15
	v_mul_f32_e32 v12, 0x3e0293ee, v13
	v_and_b32_e32 v13, 0xffff0000, v15
	v_mul_f32_e32 v13, 0x3e0293ee, v13
	v_cvt_pk_fp8_f32 v137, v12, v13 op_sel:[0,0,1]
	v_lshlrev_b32_e32 v12, 16, v8
	v_and_b32_e32 v8, 0xffff0000, v8
	v_mul_f32_e32 v138, 0x3e0293ee, v12
	v_mul_f32_e32 v8, 0x3e0293ee, v8
	v_cvt_pk_fp8_f32 v138, v138, v8
	v_lshlrev_b32_e32 v12, 16, v9
	v_and_b32_e32 v9, 0xffff0000, v9
	v_mul_f32_e32 v8, 0x3e0293ee, v12
	v_mul_f32_e32 v9, 0x3e0293ee, v9
	v_cvt_pk_fp8_f32 v138, v8, v9 op_sel:[0,0,1]
	v_lshlrev_b32_e32 v8, 16, v10
	v_mul_f32_e32 v139, 0x3e0293ee, v8
	v_and_b32_e32 v8, 0xffff0000, v10
	v_mul_f32_e32 v8, 0x3e0293ee, v8
	v_cvt_pk_fp8_f32 v139, v139, v8
	v_lshlrev_b32_e32 v9, 16, v11
	v_mul_f32_e32 v8, 0x3e0293ee, v9
	v_and_b32_e32 v9, 0xffff0000, v11
	v_mul_f32_e32 v9, 0x3e0293ee, v9
	v_cvt_pk_fp8_f32 v139, v8, v9 op_sel:[0,0,1]
	v_lshlrev_b32_e32 v8, 16, v4
	v_and_b32_e32 v4, 0xffff0000, v4
	v_mul_f32_e32 v140, 0x3e0293ee, v8
	v_mul_f32_e32 v4, 0x3e0293ee, v4
	v_cvt_pk_fp8_f32 v140, v140, v4
	v_lshlrev_b32_e32 v8, 16, v5
	v_and_b32_e32 v5, 0xffff0000, v5
	v_mul_f32_e32 v4, 0x3e0293ee, v8
	v_mul_f32_e32 v5, 0x3e0293ee, v5
	v_cvt_pk_fp8_f32 v140, v4, v5 op_sel:[0,0,1]
	v_lshlrev_b32_e32 v4, 16, v6
	v_mul_f32_e32 v141, 0x3e0293ee, v4
	v_and_b32_e32 v4, 0xffff0000, v6
	v_mul_f32_e32 v4, 0x3e0293ee, v4
	v_cvt_pk_fp8_f32 v141, v141, v4
	v_lshlrev_b32_e32 v5, 16, v7
	v_mul_f32_e32 v4, 0x3e0293ee, v5
	v_and_b32_e32 v5, 0xffff0000, v7
	v_mul_f32_e32 v5, 0x3e0293ee, v5
	v_cvt_pk_fp8_f32 v141, v4, v5 op_sel:[0,0,1]
	v_lshlrev_b32_e32 v4, 16, v0
	v_and_b32_e32 v0, 0xffff0000, v0
	v_mul_f32_e32 v142, 0x3e0293ee, v4
	v_mul_f32_e32 v0, 0x3e0293ee, v0
	v_cvt_pk_fp8_f32 v142, v142, v0
; __device__ __forceinline__ float bflo(unsigned w) { return __uint_as_float(w << 16); }
; __device__ __forceinline__ float bfhi(unsigned w) { return __uint_as_float(w & 0xffff0000u); }
; #define SBAR() __builtin_amdgcn_sched_barrier(0)
; #define SBAR() __builtin_amdgcn_sched_barrier(0)
; #define SP8_DMA_V(T) do { const unsigned char* vb_ = SP8_UNI((T).v); \
;         _Pragma("unroll") for (int i = 0; i < 8; ++i) { const unsigned char* src = vb_ + (unsigned long long)(16 * i) * SEQ + voff; \
;         __builtin_amdgcn_global_load_lds((const unsigned*)src, (LAS unsigned*)(wll + 8192 + i * 1024), 16, 0, 0); } } while (0)
; template <class P>
; __device__ __forceinline__ void sparse8_wave(P& pol, LAS unsigned char* wll, int lane) {
;     const int r32 = lane & 31, hi = lane >> 5;
;     char* wl = (char*)wll; char* Kl = wl; char* Vl = wl + 8192; float* li_l = (float*)(wl + 16384); float* al_l = li_l + 32;
;     constexpr float QCS = 0.088388347648318440f * LOG2E;
;     f32x16 o[4] = {}; float m_reg = 0.f, l_reg = 0.f; f32x16 mneg = {}; f32x16 lacc = {}; bool seen = false;
;     const i32x8 ones8 = (i32x8){0x38383838, 0x38383838, 0x38383838, 0x38383838, 0x38383838, 0x38383838, 0x38383838, 0x38383838};
;     const int a0k = 32 * ((lane >> 5) & 1) + ((lane >> 3) & 3), che = (((lane & 7) ^ (lane >> 4)) & 7) << 4, cho = che ^ 64;
;     const int vcol0 = lane >> 2; const unsigned voff = (unsigned)vcol0 * SEQ + ((((lane & 3) ^ (vcol0 >> 2)) & 3) << 4);
;     const int nt = pol.ntiles();
;     typename P::TI ti, tn;
;     ...
;     pol.tile(0, ti);
;     SP8_DMA_K(ti); SP8_DMA_V(ti);
;     pol.pre_issue(); SBAR();
;     i32x8 qf[2];
;     { const bf16_t* Qw = pol.qptr(r32); u32x4 qv[2][4];
; #pragma unroll
;       for (int sK = 0; sK < 2; ++sK)
; #pragma unroll
;           for (int c = 0; c < 4; ++c) qv[sK][c] = *(const u32x4*)(Qw + 64 * sK + 32 * hi + 8 * c);
;       SBAR();
; #pragma unroll
;       for (int sK = 0; sK < 2; ++sK) { unsigned w[8];
; #pragma unroll
;           for (int c = 0; c < 4; ++c) { const u32x4 v = qv[sK][c];
;               w[2 * c] = pk4_fp8(bflo(v.x) * QCS, bfhi(v.x) * QCS, bflo(v.y) * QCS, bfhi(v.y) * QCS); w[2 * c + 1] = pk4_fp8(bflo(v.z) * QCS, bfhi(v.z) * QCS, bflo(v.w) * QCS, bfhi(v.w) * QCS); }
;           qf[sK] = (i32x8){(int)w[0], (int)w[1], (int)w[2], (int)w[3], (int)w[4], (int)w[5], (int)w[6], (int)w[7]}; } }
	v_lshlrev_b32_e32 v4, 16, v1
	v_and_b32_e32 v1, 0xffff0000, v1
	v_mul_f32_e32 v0, 0x3e0293ee, v4
	v_mul_f32_e32 v1, 0x3e0293ee, v1
	v_cvt_pk_fp8_f32 v142, v0, v1 op_sel:[0,0,1]
	v_lshlrev_b32_e32 v0, 16, v2
	v_mul_f32_e32 v143, 0x3e0293ee, v0
	v_and_b32_e32 v0, 0xffff0000, v2
	v_mul_f32_e32 v0, 0x3e0293ee, v0
	s_add_i32 s38, s38, 1
	v_cvt_pk_fp8_f32 v143, v143, v0
	v_cvt_f32_ubyte0_e32 v0, s38
	v_exp_f32_e64 v0, -v0
	v_lshlrev_b32_e32 v1, 16, v3
	v_and_b32_e32 v2, 0xffff0000, v3
	v_mul_f32_e32 v1, 0x3e0293ee, v1
	v_mul_f32_e32 v2, 0x3e0293ee, v2
	v_or_b32_e32 v170, s57, v33
	v_cvt_pk_fp8_f32 v143, v1, v2 op_sel:[0,0,1]
	v_cvt_f32_ubyte0_e32 v1, s29
	v_mul_f32_e32 v169, 0xbfb8aa3b, v0
	v_subrev_u32_e32 v0, s25, v170
	v_cvt_f32_i32_e32 v2, v0
	v_rcp_iflag_f32_e32 v3, v1
	v_ashrrev_i32_e32 v0, 30, v0
	s_add_u32 s89, s1, s36
	v_add_u32_e32 v4, s24, v165
	v_mul_f32_e32 v3, v2, v3
	v_trunc_f32_e32 v3, v3
	v_fma_f32 v2, -v3, v1, v2
	v_cvt_i32_f32_e32 v3, v3
	v_or_b32_e32 v0, 1, v0
	v_cmp_ge_f32_e64 vcc, |v2|, v1
	s_addc_u32 s24, s33, 0
	s_add_i32 s0, s8, s55
	s_add_i32 s7, s54, s8
	v_cndmask_b32_e32 v0, 0, v0, vcc
	s_lshr_b32 s1, s0, 4
	s_bfe_u32 s0, s0, 0x30004
	s_and_b32 s7, s7, 15
	v_add_u32_e32 v0, v3, v0
	s_lshl_b32 s33, s7, 8
	s_lshl_b32 s7, s0, 3
	s_lshl_b32 s0, s0, 1
	v_sub_u32_sdwa v0, v4, sext(v0) dst_sel:DWORD dst_unused:UNUSED_PAD src0_sel:DWORD src1_sel:WORD_0
	s_sub_i32 s28, s28, s9
	s_and_b32 s29, s8, 3
	s_bfe_u32 s1, s1, 0x20001
	s_min_u32 s8, s7, 55
	s_min_u32 s9, s0, 13
	v_mul_f32_e32 v162, v169, v1
	v_cvt_f32_i32_e32 v164, v0
	v_lshlrev_b32_e32 v0, 1, v161
	v_lshrrev_b32_e32 v1, 1, v32
	s_max_u32 s6, s1, 1
	s_add_i32 s8, s8, s9
	s_min_u32 s1, s1, 2
	v_bfe_u32 v2, v32, 1, 3
	v_mov_b32_e32 v3, 0x1000
	v_lshrrev_b32_e32 v6, 2, v32
	v_bfe_u32 v7, v32, 2, 2
	v_bitop3_b32 v1, v0, v1, 7 bitop3:0x78
	s_add_i32 s8, s8, s1
	v_lshl_or_b32 v3, v163, 7, v3
	v_bitop3_b32 v6, v0, v6, 3 bitop3:0x78
	v_bitop3_b32 v7, v0, v7, 1 bitop3:0x36
	v_lshlrev_b32_e32 v173, 4, v1
	v_bitop3_b32 v1, v0, v2, 1 bitop3:0x36
	s_lshl_b32 s91, s6, 6
	s_sub_i32 s1, s8, s6
	s_max_u32 s6, s7, 1
	v_lshl_add_u32 v171, v160, 7, s61
	v_add_u32_e32 v172, s61, v3
	v_mul_i32_i24_e32 v3, 0xffffff84, v160
	v_lshlrev_b32_e32 v4, 4, v161
	v_lshl_add_u32 v5, v160, 6, s61
	v_lshlrev_b32_e32 v6, 4, v6
	v_lshlrev_b32_e32 v7, 4, v7
	v_lshlrev_b32_e32 v174, 4, v1
	v_bitop3_b32 v1, v0, v2, 4 bitop3:0x36
	v_bitop3_b32 v0, v0, v2, 5 bitop3:0x36
	s_sub_i32 s1, s1, s6
	s_max_u32 s0, s0, 1
	v_mov_b32_e32 v48, v233
	v_mov_b32_e32 v49, v233
	v_mov_b32_e32 v62, v233
	v_mov_b32_e32 v63, v233
	s_mov_b64 s[18:19], s[30:31]
	v_lshlrev_b32_e32 v175, 4, v1
	v_lshlrev_b32_e32 v176, 4, v0
	s_sub_i32 s25, s23, s60
	s_sub_i32 s23, s1, s0
	v_mov_b32_e32 v50, v233
	v_mov_b32_e32 v51, v233
	v_mov_b32_e32 v52, v233
	v_mov_b32_e32 v53, v233
	v_mov_b32_e32 v54, v233
	v_mov_b32_e32 v55, v233
	v_mov_b32_e32 v56, v233
	v_mov_b32_e32 v57, v233
	v_mov_b32_e32 v58, v233
	v_mov_b32_e32 v59, v233
	v_mov_b32_e32 v60, v233
	v_mov_b32_e32 v61, v233
	v_mov_b32_e32 v177, 0
	v_add_u32_e32 v178, v171, v3
	v_add_u32_e32 v179, s61, v4
	v_add_u32_e32 v180, v5, v6
	v_add_u32_e32 v181, v5, v7
	v_mov_b64_e32 v[78:79], v[62:63]
	v_mov_b64_e32 v[32:33], v[48:49]
	v_mov_b64_e32 v[0:1], v[48:49]
	v_mov_b64_e32 v[16:17], v[48:49]
	s_mov_b32 s30, 0x41800000
	s_mov_b32 s88, 0
	v_cmp_gt_u32_e64 s[38:39], 32, v163
	s_add_i32 s28, s28, 0x3fffffc
	s_lshl_b32 s90, s29, 10
	s_add_i32 s23, s23, 17
	s_mov_b64 s[0:1], 0
	v_mov_b64_e32 v[76:77], v[60:61]
	v_mov_b64_e32 v[74:75], v[58:59]
	v_mov_b64_e32 v[72:73], v[56:57]
	v_mov_b64_e32 v[70:71], v[54:55]
	v_mov_b64_e32 v[68:69], v[52:53]
	v_mov_b64_e32 v[66:67], v[50:51]
	v_mov_b64_e32 v[64:65], v[48:49]
	v_mov_b64_e32 v[34:35], v[50:51]
	v_mov_b64_e32 v[36:37], v[52:53]
	v_mov_b64_e32 v[38:39], v[54:55]
	v_mov_b64_e32 v[40:41], v[56:57]
	v_mov_b64_e32 v[42:43], v[58:59]
	v_mov_b64_e32 v[44:45], v[60:61]
	v_mov_b64_e32 v[46:47], v[62:63]
	v_mov_b64_e32 v[2:3], v[50:51]
	v_mov_b64_e32 v[4:5], v[52:53]
	v_mov_b64_e32 v[6:7], v[54:55]
	v_mov_b64_e32 v[8:9], v[56:57]
	v_mov_b64_e32 v[10:11], v[58:59]
	v_mov_b64_e32 v[12:13], v[60:61]
	v_mov_b64_e32 v[14:15], v[62:63]
	v_mov_b64_e32 v[18:19], v[50:51]
	v_mov_b64_e32 v[20:21], v[52:53]
	v_mov_b64_e32 v[22:23], v[54:55]
	v_mov_b64_e32 v[24:25], v[56:57]
	v_mov_b64_e32 v[26:27], v[58:59]
	v_mov_b64_e32 v[28:29], v[60:61]
	v_mov_b64_e32 v[30:31], v[62:63]
	v_mov_b32_e32 v80, 0
	v_mov_b32_e32 v81, v177
	v_mov_b32_e32 v82, v177
	v_mov_b32_e32 v83, v177
	v_mov_b32_e32 v84, v177
	v_mov_b32_e32 v85, v177
	v_mov_b32_e32 v86, v177
	v_mov_b32_e32 v87, v177
	v_mov_b32_e32 v88, v177
	v_mov_b32_e32 v89, v177
	v_mov_b32_e32 v90, v177
	v_mov_b32_e32 v91, v177
	v_mov_b32_e32 v92, v177
	v_mov_b32_e32 v93, v177
	v_mov_b32_e32 v94, v177
	v_mov_b32_e32 v95, v177
	s_mov_b32 s31, 0x41880000
	v_add_u32_e32 v216, v171, v173
	v_add_u32_e32 v217, v171, v174
	v_add_u32_e32 v218, v172, v173
	v_add_u32_e32 v219, v172, v174
	v_add_u32_e32 v220, v171, v175
	v_add_u32_e32 v221, v171, v176
	v_add_u32_e32 v222, v172, v175
	v_add_u32_e32 v223, v172, v176
	v_mov_b32_e32 v209, v208
	v_mov_b32_e32 v210, v208
	v_mov_b32_e32 v211, v208
	v_mov_b32_e32 v212, v208
	v_mov_b32_e32 v213, v208
	v_mov_b32_e32 v214, v208
	v_mov_b32_e32 v215, v208

; #define SBAR() __builtin_amdgcn_sched_barrier(0)
; #define SBAR() __builtin_amdgcn_sched_barrier(0)
; template <class P>
; __device__ __forceinline__ void sparse8_wave(P& pol, LAS unsigned char* wll, int lane) {
;     ...
;     for (int j = 0; j < nt; ++j) {
;         const bool more = (j + 1 < nt);
;         if (more) pol.tile(j + 1, tn);
;         asm volatile("s_waitcnt vmcnt(8)" ::: "memory");
;         f32x16 p0, p1;
;         { i32x8 a0[2], a1[2];
; #pragma unroll
;           for (int sK = 0; sK < 2; ++sK) { const int ch = 4 * sK + 2 * hi;
;             { const i32x4 lo = *(const i32x4*)(Kl + K8SWZ(r32, ch)), hh = *(const i32x4*)(Kl + K8SWZ(r32, ch + 1)); a0[sK] = __builtin_shufflevector(lo, hh, 0, 1, 2, 3, 4, 5, 6, 7); }
;             { const i32x4 lo = *(const i32x4*)(Kl + K8SWZ(32 + r32, ch)), hh = *(const i32x4*)(Kl + K8SWZ(32 + r32, ch + 1)); a1[sK] = __builtin_shufflevector(lo, hh, 0, 1, 2, 3, 4, 5, 6, 7); } }
;           asm volatile("s_waitcnt lgkmcnt(0)" ::: "memory"); SBAR();
;           if (more) SP8_DMA_K(tn);
;     __device__ __forceinline__ void tile(int j, TI& ti) const {
;         int dil, kt, rd; const unsigned char* vt; int voff;
;         if (j < n3) { dil = 16; kt = lo3 + j; rd = r16; vt = Vt16; voff = r16 * 256 + 64 * kt; }
;         else if (j < n3 + n2) { dil = 4; kt = lo2 + (j - n3); rd = r16 & 3; vt = Vt4; voff = rd * 1024 + 64 * kt; }
;         else { dil = 1; kt = lo1 + (j - n3 - n2); rd = 0; vt = Vt1; voff = 64 * kt; }
;         const long tok = (long)b * SEQ + dil * 64 * kt + rd;
;         ti.k = K8 + tok * 1024 + h * 128; ti.rs = (long)dil * 1024; ti.v = vt + (long)(b * 8 + h) * 128 * SEQ + voff;
;         ti.fb = (float)(64 * kt + hi32 - (512 * a + r16 + 16 * myn - rd) / dil); ti.ncd = -slope2 * (float)dil;
.LBB0_564:
	v_subrev_u32_e32 v98, s77, v170
	s_ff1_i32_b32 vcc_lo, s43
	s_mul_i32 s40, s43, s78
	v_or_b32_e32 v97, s78, v165
	s_ashr_i32 s41, s40, 31
	s_or_b32 s40, s40, s77
	v_lshrrev_b32_e32 v96, vcc_lo, v98
	s_lshl_b64 s[40:41], s[40:41], 10
	s_add_u32 s74, s89, s40
	s_addc_u32 s75, s24, s41
	s_lshl_b32 s76, s43, 10
	v_sub_u32_e32 v96, v97, v96
	v_cvt_f32_u32_e32 v97, s43
	s_add_u32 s8, s8, s72
	v_cvt_f32_i32_e32 v182, v96
	s_addc_u32 s9, s9, s73
	s_ashr_i32 s40, s42, 31
	s_add_u32 s78, s8, s42
	s_addc_u32 s79, s9, s40
	v_mul_f32_e32 v183, v169, v97
.LBB0_565:
	s_waitcnt vmcnt(8)
	ds_read_b128 v[96:99], v216
	ds_read_b128 v[100:103], v217
	ds_read_b128 v[144:147], v218
	ds_read_b128 v[148:151], v219
	ds_read_b128 v[104:107], v220
	ds_read_b128 v[108:111], v221
	ds_read_b128 v[152:155], v222
	ds_read_b128 v[156:159], v223
	s_waitcnt lgkmcnt(0)
	s_andn2_b64 s[40:41], exec, s[6:7]
	s_andn2_b64 vcc, exec, s[6:7]
	s_cbranch_vccnz .LBB0_567
	v_mul_lo_u32 v112, v166, s76
	s_lshl_b32 s6, s76, 2
	s_mov_b32 m0, s61
	v_add_u32_e32 v113, v112, v167
	s_add_u32 s6, s74, s6
	global_load_lds_dwordx4 v113, s[74:75]
	s_addc_u32 s7, s75, 0
	v_add_u32_e32 v112, v112, v168
	s_mov_b32 m0, s63
	s_nop 0
	global_load_lds_dwordx4 v112, s[6:7]
	s_lshl_b32 s6, s76, 3
	s_add_u32 s6, s74, s6
	s_addc_u32 s7, s75, 0
	s_mov_b32 m0, s64
	s_nop 0
	global_load_lds_dwordx4 v113, s[6:7]
	s_mul_i32 s6, s76, 12
	s_add_u32 s6, s74, s6
	s_addc_u32 s7, s75, 0
	s_mov_b32 m0, s65
	s_nop 0
	global_load_lds_dwordx4 v112, s[6:7]
	s_lshl_b32 s6, s76, 4
	s_add_u32 s6, s74, s6
	s_addc_u32 s7, s75, 0
	s_mov_b32 m0, s66
	s_nop 0
	global_load_lds_dwordx4 v113, s[6:7]
	s_mul_i32 s6, s76, 20
	s_add_u32 s6, s74, s6
	s_addc_u32 s7, s75, 0
	s_mov_b32 m0, s67
	s_nop 0
	global_load_lds_dwordx4 v112, s[6:7]
	s_mul_i32 s6, s76, 24
	s_add_u32 s6, s74, s6
	s_addc_u32 s7, s75, 0
	s_mov_b32 m0, s86
	s_nop 0
	global_load_lds_dwordx4 v113, s[6:7]
	s_mul_i32 s6, s76, 28
	s_add_u32 s6, s74, s6
	s_addc_u32 s7, s75, 0
	s_mov_b32 m0, s87
	s_nop 0
	global_load_lds_dwordx4 v112, s[6:7]

; __device__ __forceinline__ int crow(int r, int hi) { return (r & 3) + 8 * (r >> 2) + 4 * hi; }
; template <class P>
; __device__ __forceinline__ void sparse8_wave(P& pol, LAS unsigned char* wll, int lane) {
;     ...
;         { const bool first = (P::LSUM ? !seen : (l_reg == 0.f)) && (pmax > -INFINITY); if constexpr (P::LSUM) seen = seen || (pmax > -INFINITY);
;           const float delta = first ? pmax : (pmax > THR8 * LOG2E ? pmax : 0.f);
;           if (__any(delta != 0.f)) { alpha = first ? 1.f : __builtin_amdgcn_exp2f(-delta); m_reg += delta;
; #pragma unroll
;               for (int r = 0; r < 16; ++r) { p0[r] -= delta; p1[r] -= delta; }
;               if constexpr (!P::SPLAT) { const float nm = -m_reg;
; #pragma unroll
;                   for (int r = 0; r < 16; ++r) mneg[r] = nm; }
;               if (hi == 0) al_l[r32] = alpha; asm volatile("s_waitcnt lgkmcnt(0)" ::: "memory");
; #pragma unroll
;               for (int d = 0; d < 4; ++d)
; #pragma unroll
;                   for (int r = 0; r < 16; ++r) o[d][r] *= al_l[da::crow(r, hi)];
;               if constexpr (P::LSUM) {
; #pragma unroll
;                   for (int r = 0; r < 16; ++r) lacc[r] *= al_l[da::crow(r, hi)]; } } }
.LBB0_570:
	s_or_b64 exec, exec, s[8:9]
	s_waitcnt lgkmcnt(0)
	v_add_f32_e32 v177, v177, v96
	v_pk_add_f32 v[144:145], v[144:145], v[96:97] op_sel_hi:[1,0] neg_lo:[0,1] neg_hi:[0,1]
	v_pk_add_f32 v[148:149], v[148:149], v[96:97] op_sel_hi:[1,0] neg_lo:[0,1] neg_hi:[0,1]
	v_pk_add_f32 v[152:153], v[152:153], v[96:97] op_sel_hi:[1,0] neg_lo:[0,1] neg_hi:[0,1]
	v_pk_add_f32 v[156:157], v[156:157], v[96:97] op_sel_hi:[1,0] neg_lo:[0,1] neg_hi:[0,1]
	v_pk_add_f32 v[184:185], v[184:185], v[96:97] op_sel_hi:[1,0] neg_lo:[0,1] neg_hi:[0,1]
	v_pk_add_f32 v[188:189], v[188:189], v[96:97] op_sel_hi:[1,0] neg_lo:[0,1] neg_hi:[0,1]
	v_pk_add_f32 v[192:193], v[192:193], v[96:97] op_sel_hi:[1,0] neg_lo:[0,1] neg_hi:[0,1]
	v_pk_add_f32 v[146:147], v[146:147], v[96:97] op_sel_hi:[1,0] neg_lo:[0,1] neg_hi:[0,1]
	v_pk_add_f32 v[150:151], v[150:151], v[96:97] op_sel_hi:[1,0] neg_lo:[0,1] neg_hi:[0,1]
	v_pk_add_f32 v[154:155], v[154:155], v[96:97] op_sel_hi:[1,0] neg_lo:[0,1] neg_hi:[0,1]
	v_pk_add_f32 v[158:159], v[158:159], v[96:97] op_sel_hi:[1,0] neg_lo:[0,1] neg_hi:[0,1]
	v_pk_add_f32 v[186:187], v[186:187], v[96:97] op_sel_hi:[1,0] neg_lo:[0,1] neg_hi:[0,1]
	v_pk_add_f32 v[190:191], v[190:191], v[96:97] op_sel_hi:[1,0] neg_lo:[0,1] neg_hi:[0,1]
	v_pk_add_f32 v[194:195], v[194:195], v[96:97] op_sel_hi:[1,0] neg_lo:[0,1] neg_hi:[0,1]
	v_pk_add_f32 v[196:197], v[196:197], v[96:97] op_sel_hi:[1,0] neg_lo:[0,1] neg_hi:[0,1]
	v_sub_f32_e32 v164, v164, v96
	v_sub_f32_e32 v162, v162, v96
	ds_read_b128 v[80:83], v179 offset:16512
	ds_read_b128 v[84:87], v179 offset:16544
	ds_read_b128 v[88:91], v179 offset:16576
	ds_read_b128 v[96:99], v179 offset:16608
	v_xor_b32_e32 v95, 0x80000000, v177
	s_waitcnt lgkmcnt(0)
	v_pk_mul_f32 v[50:51], v[50:51], v[82:83]
	v_pk_mul_f32 v[52:53], v[52:53], v[84:85]
	v_pk_mul_f32 v[56:57], v[56:57], v[88:89]
	v_pk_mul_f32 v[60:61], v[60:61], v[96:97]
	v_pk_mul_f32 v[62:63], v[62:63], v[98:99]
	v_pk_mul_f32 v[58:59], v[58:59], v[90:91]
	v_pk_mul_f32 v[54:55], v[54:55], v[86:87]
	v_pk_mul_f32 v[48:49], v[48:49], v[80:81]
	v_pk_mul_f32 v[76:77], v[76:77], v[96:97]
	v_pk_mul_f32 v[72:73], v[72:73], v[88:89]
	v_pk_mul_f32 v[68:69], v[68:69], v[84:85]
	v_pk_mul_f32 v[78:79], v[78:79], v[98:99]
	v_pk_mul_f32 v[74:75], v[74:75], v[90:91]
	v_pk_mul_f32 v[70:71], v[70:71], v[86:87]
	v_pk_mul_f32 v[66:67], v[66:67], v[82:83]
	v_pk_mul_f32 v[64:65], v[64:65], v[80:81]
	v_pk_mul_f32 v[44:45], v[44:45], v[96:97]
	v_pk_mul_f32 v[40:41], v[40:41], v[88:89]
	v_pk_mul_f32 v[36:37], v[36:37], v[84:85]
	v_pk_mul_f32 v[46:47], v[46:47], v[98:99]
	v_pk_mul_f32 v[42:43], v[42:43], v[90:91]
	v_pk_mul_f32 v[38:39], v[38:39], v[86:87]
	v_pk_mul_f32 v[34:35], v[34:35], v[82:83]
	v_pk_mul_f32 v[32:33], v[32:33], v[80:81]
	v_pk_mul_f32 v[12:13], v[12:13], v[96:97]
	v_pk_mul_f32 v[8:9], v[8:9], v[88:89]
	v_pk_mul_f32 v[4:5], v[4:5], v[84:85]
	v_pk_mul_f32 v[14:15], v[14:15], v[98:99]
	v_pk_mul_f32 v[10:11], v[10:11], v[90:91]
	v_pk_mul_f32 v[6:7], v[6:7], v[86:87]
	v_pk_mul_f32 v[2:3], v[2:3], v[82:83]
	v_pk_mul_f32 v[0:1], v[0:1], v[80:81]
	v_pk_mul_f32 v[28:29], v[28:29], v[96:97]
	v_pk_mul_f32 v[24:25], v[24:25], v[88:89]
	v_pk_mul_f32 v[20:21], v[20:21], v[84:85]
	v_pk_mul_f32 v[30:31], v[30:31], v[98:99]
	v_pk_mul_f32 v[26:27], v[26:27], v[90:91]
	v_pk_mul_f32 v[22:23], v[22:23], v[86:87]
	v_pk_mul_f32 v[18:19], v[18:19], v[82:83]
	v_pk_mul_f32 v[16:17], v[16:17], v[80:81]
	v_mov_b32_e32 v94, v95
	v_mov_b64_e32 v[92:93], v[94:95]
	v_mov_b64_e32 v[90:91], v[94:95]
	v_mov_b64_e32 v[88:89], v[94:95]
	v_mov_b64_e32 v[86:87], v[94:95]
	v_mov_b64_e32 v[84:85], v[94:95]
	v_mov_b64_e32 v[82:83], v[94:95]
	v_mov_b64_e32 v[80:81], v[94:95]

; #define SBAR() __builtin_amdgcn_sched_barrier(0)
; #define SBAR() __builtin_amdgcn_sched_barrier(0)
; #define D8_MX(a, b, c) __builtin_amdgcn_mfma_scale_f32_32x32x64_f8f6f4(a, b, c, 0, 0, 0, 0, 0, 0)
; template <class P>
; __device__ __forceinline__ void sparse8_wave(P& pol, LAS unsigned char* wll, int lane) {
;     ...
;         if constexpr (P::LSUM) {
; #pragma unroll
;             for (int r = 0; r < 16; ++r) { p0[r] = __builtin_amdgcn_exp2f(p0[r]); p1[r] = __builtin_amdgcn_exp2f(p1[r]); } }
;         else { float ps = 0.f;
; #pragma unroll
;             for (int r = 0; r < 16; ++r) { p0[r] = __builtin_amdgcn_exp2f(p0[r]); p1[r] = __builtin_amdgcn_exp2f(p1[r]); ps += p0[r] + p1[r]; }
;             { auto rr = __builtin_amdgcn_permlane32_swap(__float_as_uint(ps), __float_as_uint(ps), false, false);
;               ps = __uint_as_float(rr[0]) + __uint_as_float(rr[1]); }
;             l_reg = l_reg * alpha + ps; }
;         const i32x8 pa = (i32x8){(int)pk4_fp8(p0[0], p0[1], p0[2], p0[3]), (int)pk4_fp8(p0[4], p0[5], p0[6], p0[7]), (int)pk4_fp8(p0[8], p0[9], p0[10], p0[11]), (int)pk4_fp8(p0[12], p0[13], p0[14], p0[15]),
;                                  (int)pk4_fp8(p1[0], p1[1], p1[2], p1[3]), (int)pk4_fp8(p1[4], p1[5], p1[6], p1[7]), (int)pk4_fp8(p1[8], p1[9], p1[10], p1[11]), (int)pk4_fp8(p1[12], p1[13], p1[14], p1[15])};
;         SBAR();
;         if (more) asm volatile("s_waitcnt vmcnt(8)" ::: "memory"); else asm volatile("s_waitcnt vmcnt(0)" ::: "memory");
;         SBAR();
;         { i32x8 bfr[4];
; #pragma unroll
;           for (int d0 = 0; d0 < 4; ++d0) { const int c = 32 * d0 + r32; const char* vp = Vl + c * 64; const int sw = (c >> 2) & 3;
;             const i32x4 lo = *(const i32x4*)(vp + (((2 * hi) ^ sw) << 4)), hh = *(const i32x4*)(vp + (((2 * hi + 1) ^ sw) << 4)); bfr[d0] = __builtin_shufflevector(lo, hh, 0, 1, 2, 3, 4, 5, 6, 7); }
;           asm volatile("s_waitcnt lgkmcnt(0)" ::: "memory"); SBAR();
;           if (more) SP8_DMA_V(tn);
;           SBAR();
; #pragma unroll
;           for (int d0 = 0; d0 < 4; ++d0) o[d0] = D8_MX(pa, bfr[d0], o[d0]);
;           if constexpr (P::LSUM) lacc = D8_MX(pa, ones8, lacc); }
.LBB0_577:
	v_exp_f32_e32 v198, v145
	v_exp_f32_e32 v202, v147
	v_exp_f32_e32 v144, v144
	v_exp_f32_e32 v145, v146
	v_exp_f32_e32 v146, v149
	v_exp_f32_e32 v147, v151
	v_exp_f32_e32 v149, v150
	v_exp_f32_e32 v199, v153
	v_exp_f32_e32 v203, v155
	v_exp_f32_e32 v150, v152
	v_exp_f32_e32 v151, v154
	v_exp_f32_e32 v152, v157
	v_exp_f32_e32 v154, v156
	v_exp_f32_e32 v200, v185
	v_exp_f32_e32 v204, v187
	v_exp_f32_e32 v156, v184
	v_exp_f32_e32 v157, v186
	v_exp_f32_e32 v201, v193
	v_exp_f32_e32 v205, v195
	v_exp_f32_e32 v186, v192
	v_exp_f32_e32 v187, v194
	v_exp_f32_e32 v148, v148
	v_exp_f32_e32 v153, v159
	v_exp_f32_e32 v155, v158
	v_exp_f32_e32 v158, v189
	v_exp_f32_e32 v159, v191
	v_exp_f32_e32 v184, v188
	v_exp_f32_e32 v185, v190
	v_exp_f32_e32 v188, v196
	v_exp_f32_e32 v189, v197
	v_exp_f32_e32 v164, v164
	v_exp_f32_e32 v162, v162
	v_cvt_pk_fp8_f32 v198, v198, v144
	v_cvt_pk_fp8_f32 v199, v199, v150
	v_cvt_pk_fp8_f32 v200, v200, v156
	v_cvt_pk_fp8_f32 v201, v201, v186
	v_cvt_pk_fp8_f32 v202, v202, v145
	v_cvt_pk_fp8_f32 v203, v203, v151
	v_cvt_pk_fp8_f32 v204, v204, v157
	v_cvt_pk_fp8_f32 v205, v205, v187
	s_or_b64 s[0:1], s[0:1], s[42:43]
	v_cvt_pk_fp8_f32 v198, v146, v148 op_sel:[0,0,1]
	v_cvt_pk_fp8_f32 v199, v152, v154 op_sel:[0,0,1]
	v_cvt_pk_fp8_f32 v200, v158, v184 op_sel:[0,0,1]
	v_cvt_pk_fp8_f32 v201, v188, v164 op_sel:[0,0,1]
	v_cvt_pk_fp8_f32 v202, v147, v149 op_sel:[0,0,1]
	v_cvt_pk_fp8_f32 v203, v153, v155 op_sel:[0,0,1]
	v_cvt_pk_fp8_f32 v204, v159, v185 op_sel:[0,0,1]
	v_cvt_pk_fp8_f32 v205, v189, v162 op_sel:[0,0,1]
	s_waitcnt lgkmcnt(0)
	v_mfma_f32_32x32x64_f8f6f4 v[48:63], v[198:205], v[104:111], v[48:63]
	s_add_i32 s91, s91, 64
	s_cmp_lg_u32 s23, s88
	v_mfma_f32_32x32x64_f8f6f4 v[64:79], v[198:205], v[96:103], v[64:79]
	v_mfma_f32_32x32x64_f8f6f4 v[32:47], v[198:205], v[120:127], v[32:47]
	v_mfma_f32_32x32x64_f8f6f4 v[0:15], v[198:205], v[112:119], v[0:15]
	v_mfma_f32_32x32x64_f8f6f4 v[16:31], v[198:205], v[208:215], v[16:31]
	s_cbranch_scc0 .LBB0_543
	v_mov_b32_e32 v164, v182
	v_mov_b32_e32 v162, v183
	s_branch .LBB0_555
